# barrier: first-arriving workgroup of each XCD also issues an early L2 write-back
# baseline (speedup 1.0000x reference)
; __device__ __forceinline__ unsigned xb_ld(unsigned* p)              { return __hip_atomic_load(p, __ATOMIC_RELAXED, __HIP_MEMORY_SCOPE_AGENT); }
; __device__ __forceinline__ unsigned xb_add(unsigned* p, unsigned v) { return __hip_atomic_fetch_add(p, v, __ATOMIC_RELAXED, __HIP_MEMORY_SCOPE_AGENT); }
; #define XB_SPIN(cond, bar) do { unsigned _sp = 0; while (cond) { __builtin_amdgcn_s_sleep(1); \
;     if ((++_sp & 255u) == 0u) { if (xb_ld(&(bar)[XB_TMO])) break; if (_sp > XB_SPIN_CAP) { atomicAdd(&(bar)[XB_TMO], 1u); break; } } } } while (0)
; __device__ __forceinline__ void xcd_barrier(const XcdBarrier& b) {
;     ...
;     if (threadIdx.x == 0) {
;         unsigned* bar = b.bar;
;         __builtin_amdgcn_s_waitcnt(0);
;         unsigned nloc = b.st[0], nx = b.st[1];
;         if (nloc == 0u) { xcd_barrier_complete(bar, b.x, nloc, nx); b.st[0] = nloc; b.st[1] = nx; }
;         const unsigned old = xb_add(&bar[XB_XSUB(b.x)], 1u);
;         const unsigned gen = old / nloc;
;         if (old + 1u == (gen + 1u) * nloc) {
;             __builtin_amdgcn_fence(__ATOMIC_RELEASE, "agent");
;             asm volatile("s_waitcnt vmcnt(0)" ::: "memory");
;             const unsigned og = xb_add(&bar[XB_TOP], 1u);
;             const unsigned tg = og / nx;
;             if (og + 1u == (tg + 1u) * nx) xb_add(&bar[XB_TOPGEN], 1u);
;             else XB_SPIN(xb_ld(&bar[XB_TOPGEN]) == tg, bar);
.LBB0_184:
	s_or_b64 exec, exec, s[0:1]
	s_waitcnt vmcnt(0)
	s_barrier
	s_mov_b64 s[0:1], exec
	v_readlane_b32 s2, v254, 9
	v_readlane_b32 s3, v254, 10
	s_and_b64 s[2:3], s[0:1], s[2:3]
	s_xor_b64 s[0:1], s[2:3], s[0:1]
	s_mov_b64 exec, s[2:3]
	s_cbranch_execz .LBB0_237
	s_waitcnt vmcnt(0) expcnt(0) lgkmcnt(0)
	v_mov_b32_e32 v1, 0x21000
	ds_read_b32 v2, v1
	ds_read_b32 v3, v1 offset:4
	v_readlane_b32 s2, v254, 6
	v_readlane_b32 s3, v254, 7
	v_readlane_b32 s9, v254, 8
	v_mov_b32_e32 v4, 0x1000
	v_mov_b32_e32 v5, 1
	s_lshl_b32 s9, s9, 8
	s_add_u32 s4, s2, s9
	s_addc_u32 s5, s3, 0
	global_atomic_add v4, v4, v5, s[4:5] offset:1024 sc0
	s_waitcnt vmcnt(0) lgkmcnt(0)
	v_readfirstlane_b32 s6, v4
	v_readfirstlane_b32 s7, v2
	v_readfirstlane_b32 s8, v3
	v_mov_b32_e32 v4, 0x3000
	s_nop 3
	s_mul_i32 s9, s7, 1
	s_cmp_eq_u32 s6, s9
	s_cbranch_scc0 .Lxb_ne1_0
	buffer_wbl2 sc1
.Lxb_ne1_0:
	s_mul_i32 s9, s7, 2
	s_add_u32 s6, s6, 1
	s_mul_i32 s8, s8, 2
	s_mov_b32 s10, 0
	s_cmp_lg_u32 s6, s9
	s_cbranch_scc1 .Lxb_spin_1
	buffer_wbl2 sc1
	s_waitcnt vmcnt(0)
	global_atomic_add v4, v5, s[2:3] offset:1024

; __device__ __forceinline__ unsigned xb_ld(unsigned* p)              { return __hip_atomic_load(p, __ATOMIC_RELAXED, __HIP_MEMORY_SCOPE_AGENT); }
; __device__ __forceinline__ unsigned xb_add(unsigned* p, unsigned v) { return __hip_atomic_fetch_add(p, v, __ATOMIC_RELAXED, __HIP_MEMORY_SCOPE_AGENT); }
; #define XB_SPIN(cond, bar) do { unsigned _sp = 0; while (cond) { __builtin_amdgcn_s_sleep(1); \
;     if ((++_sp & 255u) == 0u) { if (xb_ld(&(bar)[XB_TMO])) break; if (_sp > XB_SPIN_CAP) { atomicAdd(&(bar)[XB_TMO], 1u); break; } } } } while (0)
; __device__ __forceinline__ void xcd_barrier(const XcdBarrier& b) {
;     ...
;     if (threadIdx.x == 0) {
;         unsigned* bar = b.bar;
;         __builtin_amdgcn_s_waitcnt(0);
;         unsigned nloc = b.st[0], nx = b.st[1];
;         if (nloc == 0u) { xcd_barrier_complete(bar, b.x, nloc, nx); b.st[0] = nloc; b.st[1] = nx; }
;         const unsigned old = xb_add(&bar[XB_XSUB(b.x)], 1u);
;         const unsigned gen = old / nloc;
;         if (old + 1u == (gen + 1u) * nloc) {
;             __builtin_amdgcn_fence(__ATOMIC_RELEASE, "agent");
;             asm volatile("s_waitcnt vmcnt(0)" ::: "memory");
;             const unsigned og = xb_add(&bar[XB_TOP], 1u);
;             const unsigned tg = og / nx;
;             if (og + 1u == (tg + 1u) * nx) xb_add(&bar[XB_TOPGEN], 1u);
;             else XB_SPIN(xb_ld(&bar[XB_TOPGEN]) == tg, bar);
.LBB0_251:
	s_waitcnt vmcnt(0)
	s_waitcnt vmcnt(0) lgkmcnt(0)
	s_barrier
	s_mov_b64 s[0:1], exec
	v_readlane_b32 s2, v254, 9
	v_readlane_b32 s3, v254, 10
	s_and_b64 s[2:3], s[0:1], s[2:3]
	s_xor_b64 s[0:1], s[2:3], s[0:1]
	s_mov_b64 exec, s[2:3]
	s_cbranch_execz .LBB0_304
	s_waitcnt vmcnt(0) expcnt(0) lgkmcnt(0)
	v_mov_b32_e32 v1, 0x21000
	ds_read_b32 v2, v1
	ds_read_b32 v3, v1 offset:4
	v_readlane_b32 s2, v254, 6
	v_readlane_b32 s3, v254, 7
	v_readlane_b32 s9, v254, 8
	v_mov_b32_e32 v4, 0x1000
	v_mov_b32_e32 v5, 1
	s_lshl_b32 s9, s9, 8
	s_add_u32 s4, s2, s9
	s_addc_u32 s5, s3, 0
	global_atomic_add v4, v4, v5, s[4:5] offset:1024 sc0
	s_waitcnt vmcnt(0) lgkmcnt(0)
	v_readfirstlane_b32 s6, v4
	v_readfirstlane_b32 s7, v2
	v_readfirstlane_b32 s8, v3
	v_mov_b32_e32 v4, 0x3000
	s_nop 3
	s_mul_i32 s9, s7, 2
	s_cmp_eq_u32 s6, s9
	s_cbranch_scc0 .Lxb_ne2_0
	buffer_wbl2 sc1
.Lxb_ne2_0:
	s_mul_i32 s9, s7, 3
	s_add_u32 s6, s6, 1
	s_mul_i32 s8, s8, 3
	s_mov_b32 s10, 0
	s_cmp_lg_u32 s6, s9
	s_cbranch_scc1 .Lxb_spin_2
	buffer_wbl2 sc1
	s_waitcnt vmcnt(0)
	global_atomic_add v4, v5, s[2:3] offset:1024

; __device__ __forceinline__ unsigned xb_ld(unsigned* p)              { return __hip_atomic_load(p, __ATOMIC_RELAXED, __HIP_MEMORY_SCOPE_AGENT); }
; __device__ __forceinline__ unsigned xb_add(unsigned* p, unsigned v) { return __hip_atomic_fetch_add(p, v, __ATOMIC_RELAXED, __HIP_MEMORY_SCOPE_AGENT); }
; #define XB_SPIN(cond, bar) do { unsigned _sp = 0; while (cond) { __builtin_amdgcn_s_sleep(1); \
;     if ((++_sp & 255u) == 0u) { if (xb_ld(&(bar)[XB_TMO])) break; if (_sp > XB_SPIN_CAP) { atomicAdd(&(bar)[XB_TMO], 1u); break; } } } } while (0)
; __device__ __forceinline__ void xcd_barrier(const XcdBarrier& b) {
;     ...
;     if (threadIdx.x == 0) {
;         unsigned* bar = b.bar;
;         __builtin_amdgcn_s_waitcnt(0);
;         unsigned nloc = b.st[0], nx = b.st[1];
;         if (nloc == 0u) { xcd_barrier_complete(bar, b.x, nloc, nx); b.st[0] = nloc; b.st[1] = nx; }
;         const unsigned old = xb_add(&bar[XB_XSUB(b.x)], 1u);
;         const unsigned gen = old / nloc;
;         if (old + 1u == (gen + 1u) * nloc) {
;             __builtin_amdgcn_fence(__ATOMIC_RELEASE, "agent");
;             asm volatile("s_waitcnt vmcnt(0)" ::: "memory");
;             const unsigned og = xb_add(&bar[XB_TOP], 1u);
;             const unsigned tg = og / nx;
;             if (og + 1u == (tg + 1u) * nx) xb_add(&bar[XB_TOPGEN], 1u);
;             else XB_SPIN(xb_ld(&bar[XB_TOPGEN]) == tg, bar);
.LBB0_322:
	s_barrier
	s_waitcnt vmcnt(0)
	s_barrier
	s_mov_b64 s[0:1], exec
	v_readlane_b32 s2, v254, 9
	v_readlane_b32 s3, v254, 10
	s_and_b64 s[2:3], s[0:1], s[2:3]
	s_xor_b64 s[0:1], s[2:3], s[0:1]
	s_mov_b64 exec, s[2:3]
	s_cbranch_execz .LBB0_375
	s_waitcnt vmcnt(0) expcnt(0) lgkmcnt(0)
	v_mov_b32_e32 v1, 0x21000
	ds_read_b32 v2, v1
	ds_read_b32 v3, v1 offset:4
	v_readlane_b32 s2, v254, 6
	v_readlane_b32 s3, v254, 7
	v_readlane_b32 s9, v254, 8
	v_mov_b32_e32 v4, 0x1000
	v_mov_b32_e32 v5, 1
	s_lshl_b32 s9, s9, 8
	s_add_u32 s4, s2, s9
	s_addc_u32 s5, s3, 0
	global_atomic_add v4, v4, v5, s[4:5] offset:1024 sc0
	s_waitcnt vmcnt(0) lgkmcnt(0)
	v_readfirstlane_b32 s6, v4
	v_readfirstlane_b32 s7, v2
	v_readfirstlane_b32 s8, v3
	v_mov_b32_e32 v4, 0x3000
	s_nop 3
	s_mul_i32 s9, s7, 3
	s_cmp_eq_u32 s6, s9
	s_cbranch_scc0 .Lxb_ne3_0
	buffer_wbl2 sc1
.Lxb_ne3_0:
	s_mul_i32 s9, s7, 4
	s_add_u32 s6, s6, 1
	s_mul_i32 s8, s8, 4
	s_mov_b32 s10, 0
	s_cmp_lg_u32 s6, s9
	s_cbranch_scc1 .Lxb_spin_3
	buffer_wbl2 sc1
	s_waitcnt vmcnt(0)
	global_atomic_add v4, v5, s[2:3] offset:1024

; __device__ __forceinline__ unsigned xb_ld(unsigned* p)              { return __hip_atomic_load(p, __ATOMIC_RELAXED, __HIP_MEMORY_SCOPE_AGENT); }
; __device__ __forceinline__ unsigned xb_add(unsigned* p, unsigned v) { return __hip_atomic_fetch_add(p, v, __ATOMIC_RELAXED, __HIP_MEMORY_SCOPE_AGENT); }
; #define XB_SPIN(cond, bar) do { unsigned _sp = 0; while (cond) { __builtin_amdgcn_s_sleep(1); \
;     if ((++_sp & 255u) == 0u) { if (xb_ld(&(bar)[XB_TMO])) break; if (_sp > XB_SPIN_CAP) { atomicAdd(&(bar)[XB_TMO], 1u); break; } } } } while (0)
; __device__ __forceinline__ void xcd_barrier(const XcdBarrier& b) {
;     ...
;     if (threadIdx.x == 0) {
;         unsigned* bar = b.bar;
;         __builtin_amdgcn_s_waitcnt(0);
;         unsigned nloc = b.st[0], nx = b.st[1];
;         if (nloc == 0u) { xcd_barrier_complete(bar, b.x, nloc, nx); b.st[0] = nloc; b.st[1] = nx; }
;         const unsigned old = xb_add(&bar[XB_XSUB(b.x)], 1u);
;         const unsigned gen = old / nloc;
;         if (old + 1u == (gen + 1u) * nloc) {
;             __builtin_amdgcn_fence(__ATOMIC_RELEASE, "agent");
;             asm volatile("s_waitcnt vmcnt(0)" ::: "memory");
;             const unsigned og = xb_add(&bar[XB_TOP], 1u);
;             const unsigned tg = og / nx;
;             if (og + 1u == (tg + 1u) * nx) xb_add(&bar[XB_TOPGEN], 1u);
;             else XB_SPIN(xb_ld(&bar[XB_TOPGEN]) == tg, bar);
.LBB0_816:
	s_barrier
	s_waitcnt vmcnt(0)
	s_barrier
	s_mov_b64 s[0:1], exec
	v_readlane_b32 s2, v254, 9
	v_readlane_b32 s3, v254, 10
	s_and_b64 s[2:3], s[0:1], s[2:3]
	s_xor_b64 s[0:1], s[2:3], s[0:1]
	s_mov_b64 exec, s[2:3]
	s_cbranch_execz .LBB0_869
	s_waitcnt vmcnt(0) expcnt(0) lgkmcnt(0)
	v_mov_b32_e32 v1, 0x21000
	ds_read_b32 v2, v1
	ds_read_b32 v3, v1 offset:4
	v_readlane_b32 s2, v254, 6
	v_readlane_b32 s3, v254, 7
	v_readlane_b32 s9, v254, 8
	v_mov_b32_e32 v4, 0x1000
	v_mov_b32_e32 v5, 1
	s_lshl_b32 s9, s9, 8
	s_add_u32 s4, s2, s9
	s_addc_u32 s5, s3, 0
	global_atomic_add v4, v4, v5, s[4:5] offset:1024 sc0
	s_waitcnt vmcnt(0) lgkmcnt(0)
	v_readfirstlane_b32 s6, v4
	v_readfirstlane_b32 s7, v2
	v_readfirstlane_b32 s8, v3
	v_mov_b32_e32 v4, 0x3000
	s_nop 3
	s_mul_i32 s9, s7, 4
	s_cmp_eq_u32 s6, s9
	s_cbranch_scc0 .Lxb_ne4_0
	buffer_wbl2 sc1
.Lxb_ne4_0:
	s_mul_i32 s9, s7, 5
	s_add_u32 s6, s6, 1
	s_mul_i32 s8, s8, 5
	s_mov_b32 s10, 0
	s_cmp_lg_u32 s6, s9
	s_cbranch_scc1 .Lxb_spin_4
	buffer_wbl2 sc1
	s_waitcnt vmcnt(0)
	global_atomic_add v4, v5, s[2:3] offset:1024

; __device__ __forceinline__ unsigned xb_ld(unsigned* p)              { return __hip_atomic_load(p, __ATOMIC_RELAXED, __HIP_MEMORY_SCOPE_AGENT); }
; __device__ __forceinline__ unsigned xb_add(unsigned* p, unsigned v) { return __hip_atomic_fetch_add(p, v, __ATOMIC_RELAXED, __HIP_MEMORY_SCOPE_AGENT); }
; #define XB_SPIN(cond, bar) do { unsigned _sp = 0; while (cond) { __builtin_amdgcn_s_sleep(1); \
;     if ((++_sp & 255u) == 0u) { if (xb_ld(&(bar)[XB_TMO])) break; if (_sp > XB_SPIN_CAP) { atomicAdd(&(bar)[XB_TMO], 1u); break; } } } } while (0)
; __device__ __forceinline__ void xcd_barrier(const XcdBarrier& b) {
;     ...
;     if (threadIdx.x == 0) {
;         unsigned* bar = b.bar;
;         __builtin_amdgcn_s_waitcnt(0);
;         unsigned nloc = b.st[0], nx = b.st[1];
;         if (nloc == 0u) { xcd_barrier_complete(bar, b.x, nloc, nx); b.st[0] = nloc; b.st[1] = nx; }
;         const unsigned old = xb_add(&bar[XB_XSUB(b.x)], 1u);
;         const unsigned gen = old / nloc;
;         if (old + 1u == (gen + 1u) * nloc) {
;             __builtin_amdgcn_fence(__ATOMIC_RELEASE, "agent");
;             asm volatile("s_waitcnt vmcnt(0)" ::: "memory");
;             const unsigned og = xb_add(&bar[XB_TOP], 1u);
;             const unsigned tg = og / nx;
;             if (og + 1u == (tg + 1u) * nx) xb_add(&bar[XB_TOPGEN], 1u);
;             else XB_SPIN(xb_ld(&bar[XB_TOPGEN]) == tg, bar);
.LBB0_876:
	s_barrier
	s_waitcnt vmcnt(0)
	s_barrier
	s_mov_b64 s[0:1], exec
	v_readlane_b32 s2, v254, 9
	v_readlane_b32 s3, v254, 10
	s_and_b64 s[2:3], s[0:1], s[2:3]
	s_xor_b64 s[0:1], s[2:3], s[0:1]
	s_mov_b64 exec, s[2:3]
	s_cbranch_execz .LBB0_929
	s_waitcnt vmcnt(0) expcnt(0) lgkmcnt(0)
	v_mov_b32_e32 v1, 0x21000
	ds_read_b32 v2, v1
	ds_read_b32 v3, v1 offset:4
	v_readlane_b32 s2, v254, 6
	v_readlane_b32 s3, v254, 7
	v_readlane_b32 s9, v254, 8
	v_mov_b32_e32 v4, 0x1000
	v_mov_b32_e32 v5, 1
	s_lshl_b32 s9, s9, 8
	s_add_u32 s4, s2, s9
	s_addc_u32 s5, s3, 0
	global_atomic_add v4, v4, v5, s[4:5] offset:1024 sc0
	s_waitcnt vmcnt(0) lgkmcnt(0)
	v_readfirstlane_b32 s6, v4
	v_readfirstlane_b32 s7, v2
	v_readfirstlane_b32 s8, v3
	v_mov_b32_e32 v4, 0x3000
	s_nop 3
	s_mul_i32 s9, s7, 5
	s_cmp_eq_u32 s6, s9
	s_cbranch_scc0 .Lxb_ne5_0
	buffer_wbl2 sc1
.Lxb_ne5_0:
	s_mul_i32 s9, s7, 6
	s_add_u32 s6, s6, 1
	s_mul_i32 s8, s8, 6
	s_mov_b32 s10, 0
	s_cmp_lg_u32 s6, s9
	s_cbranch_scc1 .Lxb_spin_5
	buffer_wbl2 sc1
	s_waitcnt vmcnt(0)
	global_atomic_add v4, v5, s[2:3] offset:1024

; __device__ __forceinline__ unsigned xb_ld(unsigned* p)              { return __hip_atomic_load(p, __ATOMIC_RELAXED, __HIP_MEMORY_SCOPE_AGENT); }
; __device__ __forceinline__ unsigned xb_add(unsigned* p, unsigned v) { return __hip_atomic_fetch_add(p, v, __ATOMIC_RELAXED, __HIP_MEMORY_SCOPE_AGENT); }
; #define XB_SPIN(cond, bar) do { unsigned _sp = 0; while (cond) { __builtin_amdgcn_s_sleep(1); \
;     if ((++_sp & 255u) == 0u) { if (xb_ld(&(bar)[XB_TMO])) break; if (_sp > XB_SPIN_CAP) { atomicAdd(&(bar)[XB_TMO], 1u); break; } } } } while (0)
; __device__ __forceinline__ void xcd_barrier(const XcdBarrier& b) {
;     ...
;     if (threadIdx.x == 0) {
;         unsigned* bar = b.bar;
;         __builtin_amdgcn_s_waitcnt(0);
;         unsigned nloc = b.st[0], nx = b.st[1];
;         if (nloc == 0u) { xcd_barrier_complete(bar, b.x, nloc, nx); b.st[0] = nloc; b.st[1] = nx; }
;         const unsigned old = xb_add(&bar[XB_XSUB(b.x)], 1u);
;         const unsigned gen = old / nloc;
;         if (old + 1u == (gen + 1u) * nloc) {
;             __builtin_amdgcn_fence(__ATOMIC_RELEASE, "agent");
;             asm volatile("s_waitcnt vmcnt(0)" ::: "memory");
;             const unsigned og = xb_add(&bar[XB_TOP], 1u);
;             const unsigned tg = og / nx;
;             if (og + 1u == (tg + 1u) * nx) xb_add(&bar[XB_TOPGEN], 1u);
;             else XB_SPIN(xb_ld(&bar[XB_TOPGEN]) == tg, bar);
.LBB0_947:
	s_waitcnt vmcnt(0)
	s_waitcnt lgkmcnt(0)
	s_barrier
	s_mov_b64 s[0:1], exec
	v_readlane_b32 s2, v254, 9
	v_readlane_b32 s3, v254, 10
	s_and_b64 s[2:3], s[0:1], s[2:3]
	s_xor_b64 s[0:1], s[2:3], s[0:1]
	s_mov_b64 exec, s[2:3]
	s_cbranch_execz .LBB0_1000
	s_waitcnt vmcnt(0) expcnt(0) lgkmcnt(0)
	v_mov_b32_e32 v1, 0x21000
	ds_read_b32 v2, v1
	ds_read_b32 v3, v1 offset:4
	v_readlane_b32 s2, v254, 6
	v_readlane_b32 s3, v254, 7
	v_readlane_b32 s9, v254, 8
	v_mov_b32_e32 v4, 0x1000
	v_mov_b32_e32 v5, 1
	s_lshl_b32 s9, s9, 8
	s_add_u32 s4, s2, s9
	s_addc_u32 s5, s3, 0
	global_atomic_add v4, v4, v5, s[4:5] offset:1024 sc0
	s_waitcnt vmcnt(0) lgkmcnt(0)
	v_readfirstlane_b32 s6, v4
	v_readfirstlane_b32 s7, v2
	v_readfirstlane_b32 s8, v3
	v_mov_b32_e32 v4, 0x3000
	s_nop 3
	s_mul_i32 s9, s7, 6
	s_cmp_eq_u32 s6, s9
	s_cbranch_scc0 .Lxb_ne6_0
	buffer_wbl2 sc1
.Lxb_ne6_0:
	s_mul_i32 s9, s7, 7
	s_add_u32 s6, s6, 1
	s_mul_i32 s8, s8, 7
	s_mov_b32 s10, 0
	s_cmp_lg_u32 s6, s9
	s_cbranch_scc1 .Lxb_spin_6
	buffer_wbl2 sc1
	s_waitcnt vmcnt(0)
	global_atomic_add v4, v5, s[2:3] offset:1024

; __device__ __forceinline__ unsigned xb_ld(unsigned* p)              { return __hip_atomic_load(p, __ATOMIC_RELAXED, __HIP_MEMORY_SCOPE_AGENT); }
; __device__ __forceinline__ unsigned xb_add(unsigned* p, unsigned v) { return __hip_atomic_fetch_add(p, v, __ATOMIC_RELAXED, __HIP_MEMORY_SCOPE_AGENT); }
; #define XB_SPIN(cond, bar) do { unsigned _sp = 0; while (cond) { __builtin_amdgcn_s_sleep(1); \
;     if ((++_sp & 255u) == 0u) { if (xb_ld(&(bar)[XB_TMO])) break; if (_sp > XB_SPIN_CAP) { atomicAdd(&(bar)[XB_TMO], 1u); break; } } } } while (0)
; __device__ __forceinline__ void xcd_barrier(const XcdBarrier& b) {
;     ...
;     if (threadIdx.x == 0) {
;         unsigned* bar = b.bar;
;         __builtin_amdgcn_s_waitcnt(0);
;         unsigned nloc = b.st[0], nx = b.st[1];
;         if (nloc == 0u) { xcd_barrier_complete(bar, b.x, nloc, nx); b.st[0] = nloc; b.st[1] = nx; }
;         const unsigned old = xb_add(&bar[XB_XSUB(b.x)], 1u);
;         const unsigned gen = old / nloc;
;         if (old + 1u == (gen + 1u) * nloc) {
;             __builtin_amdgcn_fence(__ATOMIC_RELEASE, "agent");
;             asm volatile("s_waitcnt vmcnt(0)" ::: "memory");
;             const unsigned og = xb_add(&bar[XB_TOP], 1u);
;             const unsigned tg = og / nx;
;             if (og + 1u == (tg + 1u) * nx) xb_add(&bar[XB_TOPGEN], 1u);
;             else XB_SPIN(xb_ld(&bar[XB_TOPGEN]) == tg, bar);
.LBB0_1009:
	s_waitcnt lgkmcnt(0)
	s_barrier
	s_waitcnt vmcnt(0)
	s_barrier
	s_mov_b64 s[0:1], exec
	v_readlane_b32 s2, v254, 9
	v_readlane_b32 s3, v254, 10
	s_and_b64 s[2:3], s[0:1], s[2:3]
	s_mov_b64 exec, s[2:3]
	s_cbranch_execz .LBB0_1061
	s_waitcnt vmcnt(0) expcnt(0) lgkmcnt(0)
	v_mov_b32_e32 v1, 0x21000
	ds_read_b32 v2, v1
	ds_read_b32 v3, v1 offset:4
	v_readlane_b32 s2, v254, 6
	v_readlane_b32 s3, v254, 7
	v_readlane_b32 s9, v254, 8
	v_mov_b32_e32 v4, 0x1000
	v_mov_b32_e32 v5, 1
	s_lshl_b32 s9, s9, 8
	s_add_u32 s4, s2, s9
	s_addc_u32 s5, s3, 0
	global_atomic_add v4, v4, v5, s[4:5] offset:1024 sc0
	s_waitcnt vmcnt(0) lgkmcnt(0)
	v_readfirstlane_b32 s6, v4
	v_readfirstlane_b32 s7, v2
	v_readfirstlane_b32 s8, v3
	v_mov_b32_e32 v4, 0x3000
	s_nop 3
	s_mul_i32 s9, s7, 7
	s_cmp_eq_u32 s6, s9
	s_cbranch_scc0 .Lxb_ne7_0
	buffer_wbl2 sc1
.Lxb_ne7_0:
	s_mul_i32 s9, s7, 8
	s_add_u32 s6, s6, 1
	s_mul_i32 s8, s8, 8
	s_mov_b32 s10, 0
	s_cmp_lg_u32 s6, s9
	s_cbranch_scc1 .Lxb_spin_7
	buffer_wbl2 sc1
	s_waitcnt vmcnt(0)
	global_atomic_add v4, v5, s[2:3] offset:1024

; __device__ __forceinline__ unsigned xb_ld(unsigned* p)              { return __hip_atomic_load(p, __ATOMIC_RELAXED, __HIP_MEMORY_SCOPE_AGENT); }
; __device__ __forceinline__ unsigned xb_add(unsigned* p, unsigned v) { return __hip_atomic_fetch_add(p, v, __ATOMIC_RELAXED, __HIP_MEMORY_SCOPE_AGENT); }
; #define XB_SPIN(cond, bar) do { unsigned _sp = 0; while (cond) { __builtin_amdgcn_s_sleep(1); \
;     if ((++_sp & 255u) == 0u) { if (xb_ld(&(bar)[XB_TMO])) break; if (_sp > XB_SPIN_CAP) { atomicAdd(&(bar)[XB_TMO], 1u); break; } } } } while (0)
; __device__ __forceinline__ void xcd_barrier(const XcdBarrier& b) {
;     ...
;     if (threadIdx.x == 0) {
;         unsigned* bar = b.bar;
;         __builtin_amdgcn_s_waitcnt(0);
;         unsigned nloc = b.st[0], nx = b.st[1];
;         if (nloc == 0u) { xcd_barrier_complete(bar, b.x, nloc, nx); b.st[0] = nloc; b.st[1] = nx; }
;         const unsigned old = xb_add(&bar[XB_XSUB(b.x)], 1u);
;         const unsigned gen = old / nloc;
;         if (old + 1u == (gen + 1u) * nloc) {
;             __builtin_amdgcn_fence(__ATOMIC_RELEASE, "agent");
;             asm volatile("s_waitcnt vmcnt(0)" ::: "memory");
;             const unsigned og = xb_add(&bar[XB_TOP], 1u);
;             const unsigned tg = og / nx;
;             if (og + 1u == (tg + 1u) * nx) xb_add(&bar[XB_TOPGEN], 1u);
;             else XB_SPIN(xb_ld(&bar[XB_TOPGEN]) == tg, bar);
.Lpb8_dend:
	s_waitcnt vmcnt(0)
	s_waitcnt vmcnt(0) lgkmcnt(0)
	s_barrier
	s_mov_b64 s[0:1], exec
	v_readlane_b32 s2, v254, 9
	v_readlane_b32 s3, v254, 10
	s_and_b64 s[2:3], s[0:1], s[2:3]
	s_xor_b64 s[0:1], s[2:3], s[0:1]
	s_mov_b64 exec, s[2:3]
	s_cbranch_execz .LBB0_1152
	s_waitcnt vmcnt(0) expcnt(0) lgkmcnt(0)
	v_mov_b32_e32 v1, 0x21000
	ds_read_b32 v2, v1
	ds_read_b32 v3, v1 offset:4
	v_readlane_b32 s2, v254, 6
	v_readlane_b32 s3, v254, 7
	v_readlane_b32 s9, v254, 8
	v_mov_b32_e32 v4, 0x1000
	v_mov_b32_e32 v5, 1
	s_lshl_b32 s9, s9, 8
	s_add_u32 s4, s2, s9
	s_addc_u32 s5, s3, 0
	global_atomic_add v4, v4, v5, s[4:5] offset:1024 sc0
	s_waitcnt vmcnt(0) lgkmcnt(0)
	v_readfirstlane_b32 s6, v4
	v_readfirstlane_b32 s7, v2
	v_readfirstlane_b32 s8, v3
	v_mov_b32_e32 v4, 0x3000
	s_nop 3
	s_mul_i32 s9, s7, 8
	s_cmp_eq_u32 s6, s9
	s_cbranch_scc0 .Lxb_ne8_0
	buffer_wbl2 sc1
.Lxb_ne8_0:
	s_mul_i32 s9, s7, 9
	s_add_u32 s6, s6, 1
	s_mul_i32 s8, s8, 9
	s_mov_b32 s10, 0
	s_cmp_lg_u32 s6, s9
	s_cbranch_scc1 .Lxb_spin_8
	buffer_wbl2 sc1
	s_waitcnt vmcnt(0)
	global_atomic_add v4, v5, s[2:3] offset:1024

; __device__ __forceinline__ unsigned xb_ld(unsigned* p)              { return __hip_atomic_load(p, __ATOMIC_RELAXED, __HIP_MEMORY_SCOPE_AGENT); }
; __device__ __forceinline__ unsigned xb_add(unsigned* p, unsigned v) { return __hip_atomic_fetch_add(p, v, __ATOMIC_RELAXED, __HIP_MEMORY_SCOPE_AGENT); }
; #define XB_SPIN(cond, bar) do { unsigned _sp = 0; while (cond) { __builtin_amdgcn_s_sleep(1); \
;     if ((++_sp & 255u) == 0u) { if (xb_ld(&(bar)[XB_TMO])) break; if (_sp > XB_SPIN_CAP) { atomicAdd(&(bar)[XB_TMO], 1u); break; } } } } while (0)
; __device__ __forceinline__ void xcd_barrier(const XcdBarrier& b) {
;     ...
;     if (threadIdx.x == 0) {
;         unsigned* bar = b.bar;
;         __builtin_amdgcn_s_waitcnt(0);
;         unsigned nloc = b.st[0], nx = b.st[1];
;         if (nloc == 0u) { xcd_barrier_complete(bar, b.x, nloc, nx); b.st[0] = nloc; b.st[1] = nx; }
;         const unsigned old = xb_add(&bar[XB_XSUB(b.x)], 1u);
;         const unsigned gen = old / nloc;
;         if (old + 1u == (gen + 1u) * nloc) {
;             __builtin_amdgcn_fence(__ATOMIC_RELEASE, "agent");
;             asm volatile("s_waitcnt vmcnt(0)" ::: "memory");
;             const unsigned og = xb_add(&bar[XB_TOP], 1u);
;             const unsigned tg = og / nx;
;             if (og + 1u == (tg + 1u) * nx) xb_add(&bar[XB_TOPGEN], 1u);
;             else XB_SPIN(xb_ld(&bar[XB_TOPGEN]) == tg, bar);
.Lpb9_dend:
	s_waitcnt vmcnt(0)
	s_waitcnt vmcnt(0) lgkmcnt(0)
	s_barrier
	s_mov_b64 s[0:1], exec
	v_readlane_b32 s2, v254, 9
	v_readlane_b32 s3, v254, 10
	s_and_b64 s[2:3], s[0:1], s[2:3]
	s_xor_b64 s[0:1], s[2:3], s[0:1]
	s_mov_b64 exec, s[2:3]
	s_cbranch_execz .LBB0_1219
	s_waitcnt vmcnt(0) expcnt(0) lgkmcnt(0)
	v_mov_b32_e32 v1, 0x21000
	ds_read_b32 v2, v1
	ds_read_b32 v3, v1 offset:4
	v_readlane_b32 s2, v254, 6
	v_readlane_b32 s3, v254, 7
	v_readlane_b32 s9, v254, 8
	v_mov_b32_e32 v4, 0x1000
	v_mov_b32_e32 v5, 1
	s_lshl_b32 s9, s9, 8
	s_add_u32 s4, s2, s9
	s_addc_u32 s5, s3, 0
	global_atomic_add v4, v4, v5, s[4:5] offset:1024 sc0
	s_waitcnt vmcnt(0) lgkmcnt(0)
	v_readfirstlane_b32 s6, v4
	v_readfirstlane_b32 s7, v2
	v_readfirstlane_b32 s8, v3
	v_mov_b32_e32 v4, 0x3000
	s_nop 3
	s_mul_i32 s9, s7, 9
	s_cmp_eq_u32 s6, s9
	s_cbranch_scc0 .Lxb_ne9_0
	buffer_wbl2 sc1
.Lxb_ne9_0:
	s_mul_i32 s9, s7, 10
	s_add_u32 s6, s6, 1
	s_mul_i32 s8, s8, 10
	s_mov_b32 s10, 0
	s_cmp_lg_u32 s6, s9
	s_cbranch_scc1 .Lxb_spin_9
	buffer_wbl2 sc1
	s_waitcnt vmcnt(0)
	global_atomic_add v4, v5, s[2:3] offset:1024

; __device__ __forceinline__ unsigned xb_ld(unsigned* p)              { return __hip_atomic_load(p, __ATOMIC_RELAXED, __HIP_MEMORY_SCOPE_AGENT); }
; __device__ __forceinline__ unsigned xb_add(unsigned* p, unsigned v) { return __hip_atomic_fetch_add(p, v, __ATOMIC_RELAXED, __HIP_MEMORY_SCOPE_AGENT); }
; #define XB_SPIN(cond, bar) do { unsigned _sp = 0; while (cond) { __builtin_amdgcn_s_sleep(1); \
;     if ((++_sp & 255u) == 0u) { if (xb_ld(&(bar)[XB_TMO])) break; if (_sp > XB_SPIN_CAP) { atomicAdd(&(bar)[XB_TMO], 1u); break; } } } } while (0)
; __device__ __forceinline__ void xcd_barrier(const XcdBarrier& b) {
;     ...
;     if (threadIdx.x == 0) {
;         unsigned* bar = b.bar;
;         __builtin_amdgcn_s_waitcnt(0);
;         unsigned nloc = b.st[0], nx = b.st[1];
;         if (nloc == 0u) { xcd_barrier_complete(bar, b.x, nloc, nx); b.st[0] = nloc; b.st[1] = nx; }
;         const unsigned old = xb_add(&bar[XB_XSUB(b.x)], 1u);
;         const unsigned gen = old / nloc;
;         if (old + 1u == (gen + 1u) * nloc) {
;             __builtin_amdgcn_fence(__ATOMIC_RELEASE, "agent");
;             asm volatile("s_waitcnt vmcnt(0)" ::: "memory");
;             const unsigned og = xb_add(&bar[XB_TOP], 1u);
;             const unsigned tg = og / nx;
;             if (og + 1u == (tg + 1u) * nx) xb_add(&bar[XB_TOPGEN], 1u);
;             else XB_SPIN(xb_ld(&bar[XB_TOPGEN]) == tg, bar);
.LBB0_1229:
	s_barrier
	s_waitcnt vmcnt(0)
	s_barrier
	s_mov_b64 s[0:1], exec
	v_readlane_b32 s2, v254, 9
	v_readlane_b32 s3, v254, 10
	s_and_b64 s[2:3], s[0:1], s[2:3]
	s_mov_b64 exec, s[2:3]
	s_cbranch_execz .LBB0_1281
	s_waitcnt vmcnt(0) expcnt(0) lgkmcnt(0)
	v_mov_b32_e32 v1, 0x21000
	ds_read_b32 v2, v1
	ds_read_b32 v3, v1 offset:4
	v_readlane_b32 s2, v254, 6
	v_readlane_b32 s3, v254, 7
	v_readlane_b32 s11, v254, 8
	v_mov_b32_e32 v4, 0x1000
	v_mov_b32_e32 v5, 1
	s_lshl_b32 s11, s11, 8
	s_add_u32 s4, s2, s11
	s_addc_u32 s5, s3, 0
	global_atomic_add v4, v4, v5, s[4:5] offset:1024 sc0
	s_waitcnt vmcnt(0) lgkmcnt(0)
	v_readfirstlane_b32 s6, v4
	v_readfirstlane_b32 s7, v2
	v_readfirstlane_b32 s10, v3
	v_mov_b32_e32 v4, 0x3000
	s_nop 3
	s_mul_i32 s11, s7, 10
	s_cmp_eq_u32 s6, s11
	s_cbranch_scc0 .Lxb_ne10_0
	buffer_wbl2 sc1
.Lxb_ne10_0:
	s_mul_i32 s11, s7, 11
	s_add_u32 s6, s6, 1
	s_mul_i32 s10, s10, 11
	s_mov_b32 s12, 0
	s_cmp_lg_u32 s6, s11
	s_cbranch_scc1 .Lxb_spin_10
	buffer_wbl2 sc1
	s_waitcnt vmcnt(0)
	global_atomic_add v4, v5, s[2:3] offset:1024

; __device__ __forceinline__ unsigned xb_ld(unsigned* p)              { return __hip_atomic_load(p, __ATOMIC_RELAXED, __HIP_MEMORY_SCOPE_AGENT); }
; __device__ __forceinline__ unsigned xb_add(unsigned* p, unsigned v) { return __hip_atomic_fetch_add(p, v, __ATOMIC_RELAXED, __HIP_MEMORY_SCOPE_AGENT); }
; #define XB_SPIN(cond, bar) do { unsigned _sp = 0; while (cond) { __builtin_amdgcn_s_sleep(1); \
;     if ((++_sp & 255u) == 0u) { if (xb_ld(&(bar)[XB_TMO])) break; if (_sp > XB_SPIN_CAP) { atomicAdd(&(bar)[XB_TMO], 1u); break; } } } } while (0)
; __device__ __forceinline__ void xcd_barrier(const XcdBarrier& b) {
;     ...
;     if (threadIdx.x == 0) {
;         unsigned* bar = b.bar;
;         __builtin_amdgcn_s_waitcnt(0);
;         unsigned nloc = b.st[0], nx = b.st[1];
;         if (nloc == 0u) { xcd_barrier_complete(bar, b.x, nloc, nx); b.st[0] = nloc; b.st[1] = nx; }
;         const unsigned old = xb_add(&bar[XB_XSUB(b.x)], 1u);
;         const unsigned gen = old / nloc;
;         if (old + 1u == (gen + 1u) * nloc) {
;             __builtin_amdgcn_fence(__ATOMIC_RELEASE, "agent");
;             asm volatile("s_waitcnt vmcnt(0)" ::: "memory");
;             const unsigned og = xb_add(&bar[XB_TOP], 1u);
;             const unsigned tg = og / nx;
;             if (og + 1u == (tg + 1u) * nx) xb_add(&bar[XB_TOPGEN], 1u);
;             else XB_SPIN(xb_ld(&bar[XB_TOPGEN]) == tg, bar);
.LBB0_1295:
	s_waitcnt vmcnt(0)
	s_waitcnt vmcnt(0) lgkmcnt(0)
	s_barrier
	s_mov_b64 s[0:1], exec
	v_readlane_b32 s2, v254, 9
	v_readlane_b32 s3, v254, 10
	s_and_b64 s[2:3], s[0:1], s[2:3]
	s_xor_b64 s[0:1], s[2:3], s[0:1]
	s_mov_b64 exec, s[2:3]
	s_cbranch_execz .LBB0_1348
	s_waitcnt vmcnt(0) expcnt(0) lgkmcnt(0)
	v_mov_b32_e32 v1, 0x21000
	ds_read_b32 v2, v1
	ds_read_b32 v3, v1 offset:4
	v_readlane_b32 s2, v254, 6
	v_readlane_b32 s3, v254, 7
	v_readlane_b32 s11, v254, 8
	v_mov_b32_e32 v4, 0x1000
	v_mov_b32_e32 v5, 1
	s_lshl_b32 s11, s11, 8
	s_add_u32 s4, s2, s11
	s_addc_u32 s5, s3, 0
	global_atomic_add v4, v4, v5, s[4:5] offset:1024 sc0
	s_waitcnt vmcnt(0) lgkmcnt(0)
	v_readfirstlane_b32 s6, v4
	v_readfirstlane_b32 s7, v2
	v_readfirstlane_b32 s10, v3
	v_mov_b32_e32 v4, 0x3000
	s_nop 3
	s_mul_i32 s11, s7, 11
	s_cmp_eq_u32 s6, s11
	s_cbranch_scc0 .Lxb_ne11_0
	buffer_wbl2 sc1
.Lxb_ne11_0:
	s_mul_i32 s11, s7, 12
	s_add_u32 s6, s6, 1
	s_mul_i32 s10, s10, 12
	s_mov_b32 s12, 0
	s_cmp_lg_u32 s6, s11
	s_cbranch_scc1 .Lxb_spin_11
	buffer_wbl2 sc1
	s_waitcnt vmcnt(0)
	global_atomic_add v4, v5, s[2:3] offset:1024

; __device__ __forceinline__ unsigned xb_ld(unsigned* p)              { return __hip_atomic_load(p, __ATOMIC_RELAXED, __HIP_MEMORY_SCOPE_AGENT); }
; __device__ __forceinline__ unsigned xb_add(unsigned* p, unsigned v) { return __hip_atomic_fetch_add(p, v, __ATOMIC_RELAXED, __HIP_MEMORY_SCOPE_AGENT); }
; #define XB_SPIN(cond, bar) do { unsigned _sp = 0; while (cond) { __builtin_amdgcn_s_sleep(1); \
;     if ((++_sp & 255u) == 0u) { if (xb_ld(&(bar)[XB_TMO])) break; if (_sp > XB_SPIN_CAP) { atomicAdd(&(bar)[XB_TMO], 1u); break; } } } } while (0)
; __device__ __forceinline__ void xcd_barrier(const XcdBarrier& b) {
;     ...
;     if (threadIdx.x == 0) {
;         unsigned* bar = b.bar;
;         __builtin_amdgcn_s_waitcnt(0);
;         unsigned nloc = b.st[0], nx = b.st[1];
;         if (nloc == 0u) { xcd_barrier_complete(bar, b.x, nloc, nx); b.st[0] = nloc; b.st[1] = nx; }
;         const unsigned old = xb_add(&bar[XB_XSUB(b.x)], 1u);
;         const unsigned gen = old / nloc;
;         if (old + 1u == (gen + 1u) * nloc) {
;             __builtin_amdgcn_fence(__ATOMIC_RELEASE, "agent");
;             asm volatile("s_waitcnt vmcnt(0)" ::: "memory");
;             const unsigned og = xb_add(&bar[XB_TOP], 1u);
;             const unsigned tg = og / nx;
;             if (og + 1u == (tg + 1u) * nx) xb_add(&bar[XB_TOPGEN], 1u);
;             else XB_SPIN(xb_ld(&bar[XB_TOPGEN]) == tg, bar);
.LBB0_1389:
	s_barrier
	s_waitcnt vmcnt(0)
	s_barrier
	s_mov_b64 s[0:1], exec
	v_readlane_b32 s2, v254, 9
	v_readlane_b32 s3, v254, 10
	s_and_b64 s[2:3], s[0:1], s[2:3]
	s_mov_b64 exec, s[2:3]
	s_cbranch_execz .LBB0_1441
	s_waitcnt vmcnt(0) expcnt(0) lgkmcnt(0)
	v_mov_b32_e32 v1, 0x21000
	ds_read_b32 v2, v1
	ds_read_b32 v3, v1 offset:4
	v_readlane_b32 s2, v254, 6
	v_readlane_b32 s3, v254, 7
	v_readlane_b32 s11, v254, 8
	v_mov_b32_e32 v4, 0x1000
	v_mov_b32_e32 v5, 1
	s_lshl_b32 s11, s11, 8
	s_add_u32 s4, s2, s11
	s_addc_u32 s5, s3, 0
	global_atomic_add v4, v4, v5, s[4:5] offset:1024 sc0
	s_waitcnt vmcnt(0) lgkmcnt(0)
	v_readfirstlane_b32 s6, v4
	v_readfirstlane_b32 s7, v2
	v_readfirstlane_b32 s10, v3
	v_mov_b32_e32 v4, 0x3000
	s_nop 3
	s_mul_i32 s11, s7, 12
	s_cmp_eq_u32 s6, s11
	s_cbranch_scc0 .Lxb_ne12_0
	buffer_wbl2 sc1
.Lxb_ne12_0:
	s_mul_i32 s11, s7, 13
	s_add_u32 s6, s6, 1
	s_mul_i32 s10, s10, 13
	s_mov_b32 s12, 0
	s_cmp_lg_u32 s6, s11
	s_cbranch_scc1 .Lxb_spin_12
	buffer_wbl2 sc1
	s_waitcnt vmcnt(0)
	global_atomic_add v4, v5, s[2:3] offset:1024

; __device__ __forceinline__ unsigned xb_ld(unsigned* p)              { return __hip_atomic_load(p, __ATOMIC_RELAXED, __HIP_MEMORY_SCOPE_AGENT); }
; __device__ __forceinline__ unsigned xb_add(unsigned* p, unsigned v) { return __hip_atomic_fetch_add(p, v, __ATOMIC_RELAXED, __HIP_MEMORY_SCOPE_AGENT); }
; #define XB_SPIN(cond, bar) do { unsigned _sp = 0; while (cond) { __builtin_amdgcn_s_sleep(1); \
;     if ((++_sp & 255u) == 0u) { if (xb_ld(&(bar)[XB_TMO])) break; if (_sp > XB_SPIN_CAP) { atomicAdd(&(bar)[XB_TMO], 1u); break; } } } } while (0)
; __device__ __forceinline__ void xcd_barrier(const XcdBarrier& b) {
;     ...
;     if (threadIdx.x == 0) {
;         unsigned* bar = b.bar;
;         __builtin_amdgcn_s_waitcnt(0);
;         unsigned nloc = b.st[0], nx = b.st[1];
;         if (nloc == 0u) { xcd_barrier_complete(bar, b.x, nloc, nx); b.st[0] = nloc; b.st[1] = nx; }
;         const unsigned old = xb_add(&bar[XB_XSUB(b.x)], 1u);
;         const unsigned gen = old / nloc;
;         if (old + 1u == (gen + 1u) * nloc) {
;             __builtin_amdgcn_fence(__ATOMIC_RELEASE, "agent");
;             asm volatile("s_waitcnt vmcnt(0)" ::: "memory");
;             const unsigned og = xb_add(&bar[XB_TOP], 1u);
;             const unsigned tg = og / nx;
;             if (og + 1u == (tg + 1u) * nx) xb_add(&bar[XB_TOPGEN], 1u);
;             else XB_SPIN(xb_ld(&bar[XB_TOPGEN]) == tg, bar);
.LBB0_1447:
	s_or_b64 exec, exec, s[2:3]
	s_waitcnt vmcnt(0)
	s_barrier
	s_mov_b64 s[0:1], exec
	v_readlane_b32 s2, v254, 9
	v_readlane_b32 s3, v254, 10
	s_and_b64 s[2:3], s[0:1], s[2:3]
	s_mov_b64 exec, s[2:3]
	s_cbranch_execz .LBB0_1499
	s_waitcnt vmcnt(0) expcnt(0) lgkmcnt(0)
	v_mov_b32_e32 v1, 0x21000
	ds_read_b32 v2, v1
	ds_read_b32 v3, v1 offset:4
	v_readlane_b32 s2, v254, 6
	v_readlane_b32 s3, v254, 7
	v_readlane_b32 s11, v254, 8
	v_mov_b32_e32 v4, 0x1000
	v_mov_b32_e32 v5, 1
	s_lshl_b32 s11, s11, 8
	s_add_u32 s4, s2, s11
	s_addc_u32 s5, s3, 0
	global_atomic_add v4, v4, v5, s[4:5] offset:1024 sc0
	s_waitcnt vmcnt(0) lgkmcnt(0)
	v_readfirstlane_b32 s6, v4
	v_readfirstlane_b32 s7, v2
	v_readfirstlane_b32 s10, v3
	v_mov_b32_e32 v4, 0x3000
	s_nop 3
	s_mul_i32 s11, s7, 13
	s_cmp_eq_u32 s6, s11
	s_cbranch_scc0 .Lxb_ne13_0
	buffer_wbl2 sc1
.Lxb_ne13_0:
	s_mul_i32 s11, s7, 14
	s_add_u32 s6, s6, 1
	s_mul_i32 s10, s10, 14
	s_mov_b32 s12, 0
	s_cmp_lg_u32 s6, s11
	s_cbranch_scc1 .Lxb_spin_13
	buffer_wbl2 sc1
	s_waitcnt vmcnt(0)
	global_atomic_add v4, v5, s[2:3] offset:1024

; __device__ __forceinline__ unsigned xb_ld(unsigned* p)              { return __hip_atomic_load(p, __ATOMIC_RELAXED, __HIP_MEMORY_SCOPE_AGENT); }
; __device__ __forceinline__ unsigned xb_add(unsigned* p, unsigned v) { return __hip_atomic_fetch_add(p, v, __ATOMIC_RELAXED, __HIP_MEMORY_SCOPE_AGENT); }
; #define XB_SPIN(cond, bar) do { unsigned _sp = 0; while (cond) { __builtin_amdgcn_s_sleep(1); \
;     if ((++_sp & 255u) == 0u) { if (xb_ld(&(bar)[XB_TMO])) break; if (_sp > XB_SPIN_CAP) { atomicAdd(&(bar)[XB_TMO], 1u); break; } } } } while (0)
; __device__ __forceinline__ void xcd_barrier(const XcdBarrier& b) {
;     ...
;     if (threadIdx.x == 0) {
;         unsigned* bar = b.bar;
;         __builtin_amdgcn_s_waitcnt(0);
;         unsigned nloc = b.st[0], nx = b.st[1];
;         if (nloc == 0u) { xcd_barrier_complete(bar, b.x, nloc, nx); b.st[0] = nloc; b.st[1] = nx; }
;         const unsigned old = xb_add(&bar[XB_XSUB(b.x)], 1u);
;         const unsigned gen = old / nloc;
;         if (old + 1u == (gen + 1u) * nloc) {
;             __builtin_amdgcn_fence(__ATOMIC_RELEASE, "agent");
;             asm volatile("s_waitcnt vmcnt(0)" ::: "memory");
;             const unsigned og = xb_add(&bar[XB_TOP], 1u);
;             const unsigned tg = og / nx;
;             if (og + 1u == (tg + 1u) * nx) xb_add(&bar[XB_TOPGEN], 1u);
;             else XB_SPIN(xb_ld(&bar[XB_TOPGEN]) == tg, bar);
.LBB0_1614:
	s_barrier
	s_waitcnt vmcnt(0)
	s_barrier
	s_mov_b64 s[0:1], exec
	v_readlane_b32 s2, v254, 9
	v_readlane_b32 s3, v254, 10
	s_and_b64 s[2:3], s[0:1], s[2:3]
	s_mov_b64 exec, s[2:3]
	s_cbranch_execz .LBB0_1666
	s_waitcnt vmcnt(0) expcnt(0) lgkmcnt(0)
	v_mov_b32_e32 v1, 0x21000
	ds_read_b32 v2, v1
	ds_read_b32 v3, v1 offset:4
	v_readlane_b32 s2, v254, 6
	v_readlane_b32 s3, v254, 7
	v_readlane_b32 s11, v254, 8
	v_mov_b32_e32 v4, 0x1000
	v_mov_b32_e32 v5, 1
	s_lshl_b32 s11, s11, 8
	s_add_u32 s4, s2, s11
	s_addc_u32 s5, s3, 0
	global_atomic_add v4, v4, v5, s[4:5] offset:1024 sc0
	s_waitcnt vmcnt(0) lgkmcnt(0)
	v_readfirstlane_b32 s6, v4
	v_readfirstlane_b32 s7, v2
	v_readfirstlane_b32 s10, v3
	v_mov_b32_e32 v4, 0x3000
	s_nop 3
	s_mul_i32 s11, s7, 14
	s_cmp_eq_u32 s6, s11
	s_cbranch_scc0 .Lxb_ne14_0
	buffer_wbl2 sc1
.Lxb_ne14_0:
	s_mul_i32 s11, s7, 15
	s_add_u32 s6, s6, 1
	s_mul_i32 s10, s10, 15
	s_mov_b32 s12, 0
	s_cmp_lg_u32 s6, s11
	s_cbranch_scc1 .Lxb_spin_14
	buffer_wbl2 sc1
	s_waitcnt vmcnt(0)
	global_atomic_add v4, v5, s[2:3] offset:1024

; __device__ __forceinline__ unsigned xb_ld(unsigned* p)              { return __hip_atomic_load(p, __ATOMIC_RELAXED, __HIP_MEMORY_SCOPE_AGENT); }
; __device__ __forceinline__ unsigned xb_add(unsigned* p, unsigned v) { return __hip_atomic_fetch_add(p, v, __ATOMIC_RELAXED, __HIP_MEMORY_SCOPE_AGENT); }
; #define XB_SPIN(cond, bar) do { unsigned _sp = 0; while (cond) { __builtin_amdgcn_s_sleep(1); \
;     if ((++_sp & 255u) == 0u) { if (xb_ld(&(bar)[XB_TMO])) break; if (_sp > XB_SPIN_CAP) { atomicAdd(&(bar)[XB_TMO], 1u); break; } } } } while (0)
; __device__ __forceinline__ void xcd_barrier(const XcdBarrier& b) {
;     ...
;     if (threadIdx.x == 0) {
;         unsigned* bar = b.bar;
;         __builtin_amdgcn_s_waitcnt(0);
;         unsigned nloc = b.st[0], nx = b.st[1];
;         if (nloc == 0u) { xcd_barrier_complete(bar, b.x, nloc, nx); b.st[0] = nloc; b.st[1] = nx; }
;         const unsigned old = xb_add(&bar[XB_XSUB(b.x)], 1u);
;         const unsigned gen = old / nloc;
;         if (old + 1u == (gen + 1u) * nloc) {
;             __builtin_amdgcn_fence(__ATOMIC_RELEASE, "agent");
;             asm volatile("s_waitcnt vmcnt(0)" ::: "memory");
;             const unsigned og = xb_add(&bar[XB_TOP], 1u);
;             const unsigned tg = og / nx;
;             if (og + 1u == (tg + 1u) * nx) xb_add(&bar[XB_TOPGEN], 1u);
;             else XB_SPIN(xb_ld(&bar[XB_TOPGEN]) == tg, bar);
.LBB0_1684:
	s_waitcnt vmcnt(0)
	s_waitcnt lgkmcnt(0)
	s_barrier
	s_mov_b64 s[0:1], exec
	v_readlane_b32 s2, v254, 9
	v_readlane_b32 s3, v254, 10
	s_and_b64 s[2:3], s[0:1], s[2:3]
	s_xor_b64 s[0:1], s[2:3], s[0:1]
	s_mov_b64 exec, s[2:3]
	s_cbranch_execz .LBB0_1737
	s_waitcnt vmcnt(0) expcnt(0) lgkmcnt(0)
	v_mov_b32_e32 v1, 0x21000
	ds_read_b32 v2, v1
	ds_read_b32 v3, v1 offset:4
	v_readlane_b32 s2, v254, 6
	v_readlane_b32 s3, v254, 7
	v_readlane_b32 s11, v254, 8
	v_mov_b32_e32 v4, 0x1000
	v_mov_b32_e32 v5, 1
	s_lshl_b32 s11, s11, 8
	s_add_u32 s4, s2, s11
	s_addc_u32 s5, s3, 0
	global_atomic_add v4, v4, v5, s[4:5] offset:1024 sc0
	s_waitcnt vmcnt(0) lgkmcnt(0)
	v_readfirstlane_b32 s6, v4
	v_readfirstlane_b32 s7, v2
	v_readfirstlane_b32 s10, v3
	v_mov_b32_e32 v4, 0x3000
	s_nop 3
	s_mul_i32 s11, s7, 15
	s_cmp_eq_u32 s6, s11
	s_cbranch_scc0 .Lxb_ne15_0
	buffer_wbl2 sc1
.Lxb_ne15_0:
	s_mul_i32 s11, s7, 16
	s_add_u32 s6, s6, 1
	s_mul_i32 s10, s10, 16
	s_mov_b32 s12, 0
	s_cmp_lg_u32 s6, s11
	s_cbranch_scc1 .Lxb_spin_15
	buffer_wbl2 sc1
	s_waitcnt vmcnt(0)
	global_atomic_add v4, v5, s[2:3] offset:1024

; __device__ __forceinline__ unsigned xb_ld(unsigned* p)              { return __hip_atomic_load(p, __ATOMIC_RELAXED, __HIP_MEMORY_SCOPE_AGENT); }
; __device__ __forceinline__ unsigned xb_add(unsigned* p, unsigned v) { return __hip_atomic_fetch_add(p, v, __ATOMIC_RELAXED, __HIP_MEMORY_SCOPE_AGENT); }
; #define XB_SPIN(cond, bar) do { unsigned _sp = 0; while (cond) { __builtin_amdgcn_s_sleep(1); \
;     if ((++_sp & 255u) == 0u) { if (xb_ld(&(bar)[XB_TMO])) break; if (_sp > XB_SPIN_CAP) { atomicAdd(&(bar)[XB_TMO], 1u); break; } } } } while (0)
; __device__ __forceinline__ void xcd_barrier(const XcdBarrier& b) {
;     ...
;     if (threadIdx.x == 0) {
;         unsigned* bar = b.bar;
;         __builtin_amdgcn_s_waitcnt(0);
;         unsigned nloc = b.st[0], nx = b.st[1];
;         if (nloc == 0u) { xcd_barrier_complete(bar, b.x, nloc, nx); b.st[0] = nloc; b.st[1] = nx; }
;         const unsigned old = xb_add(&bar[XB_XSUB(b.x)], 1u);
;         const unsigned gen = old / nloc;
;         if (old + 1u == (gen + 1u) * nloc) {
;             __builtin_amdgcn_fence(__ATOMIC_RELEASE, "agent");
;             asm volatile("s_waitcnt vmcnt(0)" ::: "memory");
;             const unsigned og = xb_add(&bar[XB_TOP], 1u);
;             const unsigned tg = og / nx;
;             if (og + 1u == (tg + 1u) * nx) xb_add(&bar[XB_TOPGEN], 1u);
;             else XB_SPIN(xb_ld(&bar[XB_TOPGEN]) == tg, bar);
.LBB0_1746:
	s_waitcnt lgkmcnt(0)
	s_barrier
	s_waitcnt vmcnt(0)
	s_barrier
	s_mov_b64 s[0:1], exec
	v_readlane_b32 s2, v254, 9
	v_readlane_b32 s3, v254, 10
	s_and_b64 s[2:3], s[0:1], s[2:3]
	s_mov_b64 exec, s[2:3]
	s_cbranch_execz .LBB0_1798
	s_waitcnt vmcnt(0) expcnt(0) lgkmcnt(0)
	v_mov_b32_e32 v1, 0x21000
	ds_read_b32 v2, v1
	ds_read_b32 v3, v1 offset:4
	v_readlane_b32 s2, v254, 6
	v_readlane_b32 s3, v254, 7
	v_readlane_b32 s9, v254, 8
	v_mov_b32_e32 v4, 0x1000
	v_mov_b32_e32 v5, 1
	s_lshl_b32 s9, s9, 8
	s_add_u32 s4, s2, s9
	s_addc_u32 s5, s3, 0
	global_atomic_add v4, v4, v5, s[4:5] offset:1024 sc0
	s_waitcnt vmcnt(0) lgkmcnt(0)
	v_readfirstlane_b32 s6, v4
	v_readfirstlane_b32 s7, v2
	v_readfirstlane_b32 s8, v3
	v_mov_b32_e32 v4, 0x3000
	s_nop 3
	s_mul_i32 s9, s7, 16
	s_cmp_eq_u32 s6, s9
	s_cbranch_scc0 .Lxb_ne16_0
	buffer_wbl2 sc1
.Lxb_ne16_0:
	s_mul_i32 s9, s7, 17
	s_add_u32 s6, s6, 1
	s_mul_i32 s8, s8, 17
	s_mov_b32 s10, 0
	s_cmp_lg_u32 s6, s9
	s_cbranch_scc1 .Lxb_spin_16
	buffer_wbl2 sc1
	s_waitcnt vmcnt(0)
	global_atomic_add v4, v5, s[2:3] offset:1024

; __device__ __forceinline__ unsigned xb_ld(unsigned* p)              { return __hip_atomic_load(p, __ATOMIC_RELAXED, __HIP_MEMORY_SCOPE_AGENT); }
; __device__ __forceinline__ unsigned xb_add(unsigned* p, unsigned v) { return __hip_atomic_fetch_add(p, v, __ATOMIC_RELAXED, __HIP_MEMORY_SCOPE_AGENT); }
; #define XB_SPIN(cond, bar) do { unsigned _sp = 0; while (cond) { __builtin_amdgcn_s_sleep(1); \
;     if ((++_sp & 255u) == 0u) { if (xb_ld(&(bar)[XB_TMO])) break; if (_sp > XB_SPIN_CAP) { atomicAdd(&(bar)[XB_TMO], 1u); break; } } } } while (0)
; __device__ __forceinline__ void xcd_barrier(const XcdBarrier& b) {
;     ...
;     if (threadIdx.x == 0) {
;         unsigned* bar = b.bar;
;         __builtin_amdgcn_s_waitcnt(0);
;         unsigned nloc = b.st[0], nx = b.st[1];
;         if (nloc == 0u) { xcd_barrier_complete(bar, b.x, nloc, nx); b.st[0] = nloc; b.st[1] = nx; }
;         const unsigned old = xb_add(&bar[XB_XSUB(b.x)], 1u);
;         const unsigned gen = old / nloc;
;         if (old + 1u == (gen + 1u) * nloc) {
;             __builtin_amdgcn_fence(__ATOMIC_RELEASE, "agent");
;             asm volatile("s_waitcnt vmcnt(0)" ::: "memory");
;             const unsigned og = xb_add(&bar[XB_TOP], 1u);
;             const unsigned tg = og / nx;
;             if (og + 1u == (tg + 1u) * nx) xb_add(&bar[XB_TOPGEN], 1u);
;             else XB_SPIN(xb_ld(&bar[XB_TOPGEN]) == tg, bar);
.Lpb17_dend:
	s_waitcnt vmcnt(0)
	s_waitcnt vmcnt(0) lgkmcnt(0)
	s_barrier
	s_mov_b64 s[0:1], exec
	v_readlane_b32 s2, v254, 9
	v_readlane_b32 s3, v254, 10
	s_and_b64 s[2:3], s[0:1], s[2:3]
	s_xor_b64 s[0:1], s[2:3], s[0:1]
	s_mov_b64 exec, s[2:3]
	s_cbranch_execz .LBB0_1889
	s_waitcnt vmcnt(0) expcnt(0) lgkmcnt(0)
	v_mov_b32_e32 v1, 0x21000
	ds_read_b32 v2, v1
	ds_read_b32 v3, v1 offset:4
	v_readlane_b32 s2, v254, 6
	v_readlane_b32 s3, v254, 7
	v_readlane_b32 s9, v254, 8
	v_mov_b32_e32 v4, 0x1000
	v_mov_b32_e32 v5, 1
	s_lshl_b32 s9, s9, 8
	s_add_u32 s4, s2, s9
	s_addc_u32 s5, s3, 0
	global_atomic_add v4, v4, v5, s[4:5] offset:1024 sc0
	s_waitcnt vmcnt(0) lgkmcnt(0)
	v_readfirstlane_b32 s6, v4
	v_readfirstlane_b32 s7, v2
	v_readfirstlane_b32 s8, v3
	v_mov_b32_e32 v4, 0x3000
	s_nop 3
	s_mul_i32 s9, s7, 17
	s_cmp_eq_u32 s6, s9
	s_cbranch_scc0 .Lxb_ne17_0
	buffer_wbl2 sc1
.Lxb_ne17_0:
	s_mul_i32 s9, s7, 18
	s_add_u32 s6, s6, 1
	s_mul_i32 s8, s8, 18
	s_mov_b32 s10, 0
	s_cmp_lg_u32 s6, s9
	s_cbranch_scc1 .Lxb_spin_17
	buffer_wbl2 sc1
	s_waitcnt vmcnt(0)
	global_atomic_add v4, v5, s[2:3] offset:1024

; __device__ __forceinline__ unsigned xb_ld(unsigned* p)              { return __hip_atomic_load(p, __ATOMIC_RELAXED, __HIP_MEMORY_SCOPE_AGENT); }
; __device__ __forceinline__ unsigned xb_add(unsigned* p, unsigned v) { return __hip_atomic_fetch_add(p, v, __ATOMIC_RELAXED, __HIP_MEMORY_SCOPE_AGENT); }
; #define XB_SPIN(cond, bar) do { unsigned _sp = 0; while (cond) { __builtin_amdgcn_s_sleep(1); \
;     if ((++_sp & 255u) == 0u) { if (xb_ld(&(bar)[XB_TMO])) break; if (_sp > XB_SPIN_CAP) { atomicAdd(&(bar)[XB_TMO], 1u); break; } } } } while (0)
; __device__ __forceinline__ void xcd_barrier(const XcdBarrier& b) {
;     ...
;     if (threadIdx.x == 0) {
;         unsigned* bar = b.bar;
;         __builtin_amdgcn_s_waitcnt(0);
;         unsigned nloc = b.st[0], nx = b.st[1];
;         if (nloc == 0u) { xcd_barrier_complete(bar, b.x, nloc, nx); b.st[0] = nloc; b.st[1] = nx; }
;         const unsigned old = xb_add(&bar[XB_XSUB(b.x)], 1u);
;         const unsigned gen = old / nloc;
;         if (old + 1u == (gen + 1u) * nloc) {
;             __builtin_amdgcn_fence(__ATOMIC_RELEASE, "agent");
;             asm volatile("s_waitcnt vmcnt(0)" ::: "memory");
;             const unsigned og = xb_add(&bar[XB_TOP], 1u);
;             const unsigned tg = og / nx;
;             if (og + 1u == (tg + 1u) * nx) xb_add(&bar[XB_TOPGEN], 1u);
;             else XB_SPIN(xb_ld(&bar[XB_TOPGEN]) == tg, bar);
.LBB0_1903:
	s_waitcnt vmcnt(0)
	s_waitcnt vmcnt(0) lgkmcnt(0)
	s_barrier
	s_mov_b64 s[0:1], exec
	v_readlane_b32 s2, v254, 9
	v_readlane_b32 s3, v254, 10
	s_and_b64 s[2:3], s[0:1], s[2:3]
	s_xor_b64 s[0:1], s[2:3], s[0:1]
	s_mov_b64 exec, s[2:3]
	s_cbranch_execz .LBB0_1956
	s_waitcnt vmcnt(0) expcnt(0) lgkmcnt(0)
	v_mov_b32_e32 v1, 0x21000
	ds_read_b32 v2, v1
	ds_read_b32 v3, v1 offset:4
	v_readlane_b32 s2, v254, 6
	v_readlane_b32 s3, v254, 7
	v_readlane_b32 s9, v254, 8
	v_mov_b32_e32 v4, 0x1000
	v_mov_b32_e32 v5, 1
	s_lshl_b32 s9, s9, 8
	s_add_u32 s4, s2, s9
	s_addc_u32 s5, s3, 0
	global_atomic_add v4, v4, v5, s[4:5] offset:1024 sc0
	s_waitcnt vmcnt(0) lgkmcnt(0)
	v_readfirstlane_b32 s6, v4
	v_readfirstlane_b32 s7, v2
	v_readfirstlane_b32 s8, v3
	v_mov_b32_e32 v4, 0x3000
	s_nop 3
	s_mul_i32 s9, s7, 18
	s_cmp_eq_u32 s6, s9
	s_cbranch_scc0 .Lxb_ne18_0
	buffer_wbl2 sc1
.Lxb_ne18_0:
	s_mul_i32 s9, s7, 19
	s_add_u32 s6, s6, 1
	s_mul_i32 s8, s8, 19
	s_mov_b32 s10, 0
	s_cmp_lg_u32 s6, s9
	s_cbranch_scc1 .Lxb_spin_18
	buffer_wbl2 sc1
	s_waitcnt vmcnt(0)
	global_atomic_add v4, v5, s[2:3] offset:1024
